# baseline (speedup 1.0000x reference)
.Lagg2_nospecb:
	s_mov_b64 exec, s[4:5]
	global_load_dwordx2 v[8:9], v[8:9], off
	s_add_u32 s0, s40, s0
	s_addc_u32 s1, s41, s1
	s_load_dword s33, s[0:1], 0x0
	s_min_i32 s0, s52, 0xc340
	s_ashr_i32 s1, s0, 31
	s_lshl_b64 s[0:1], s[0:1], 2
	s_add_u32 s0, s42, s0
	s_addc_u32 s1, s43, s1
	s_load_dword s53, s[0:1], 0x3c
	v_and_b32_e32 v1, 15, v0
	v_lshrrev_b32_e32 v23, 4, v0
	v_lshlrev_b32_e32 v24, 4, v1
	s_waitcnt lgkmcnt(0)
	s_cmp_ge_i32 s33, s53
	s_nop 0
	s_cbranch_scc1 .Lagg2_empty
	v_mov_b32_e32 v2, 0x4400
	v_lshl_or_b32 v42, v0, 2, v2
	v_lshl_or_b32 v43, v23, 2, v2
	v_mov_b32_e32 v2, 0x2200
	v_or_b32_e32 v25, 0x3400, v24
	v_cmp_eq_u32_e64 s[0:1], 0, v1
	v_cmp_eq_u32_e64 s[2:3], 1, v23
	v_cmp_eq_u32_e64 s[4:5], 2, v23
	v_cmp_eq_u32_e64 s[6:7], 3, v23
	v_cmp_eq_u32_e64 s[8:9], 4, v23
	v_cmp_eq_u32_e64 s[10:11], 5, v23
	v_cmp_eq_u32_e64 s[12:13], 6, v23
	v_cmp_eq_u32_e64 s[14:15], 7, v23
	v_cmp_eq_u32_e64 s[16:17], 8, v23
	v_cmp_eq_u32_e64 s[18:19], 9, v23
	v_cmp_eq_u32_e64 s[20:21], 10, v23
	v_cmp_eq_u32_e64 s[22:23], 11, v23
	v_cmp_eq_u32_e64 s[24:25], 12, v23
	v_cmp_eq_u32_e64 s[26:27], 13, v23
	v_cmp_eq_u32_e64 s[28:29], 14, v23
	v_cmp_eq_u32_e64 s[30:31], 15, v23
	v_add_u32_e32 v26, s33, v0
	v_lshl_add_u32 v44, v0, 3, v2
	v_mov_b32_e32 v45, 0
	s_movk_i32 s66, 0x110
	v_mov_b32_e32 v46, -1
	s_mov_b64 s[40:41], 0x800
	s_mov_b32 s67, 0xffff0
	v_mov_b32_e32 v47, 2
	s_mov_b32 s68, s33
	s_branch .LBB2_8

.Lagg3_nospecb:
	s_mov_b64 exec, s[4:5]
	global_load_dwordx2 v[8:9], v[8:9], off
	s_add_u32 s0, s40, s0
	s_addc_u32 s1, s41, s1
	s_load_dword s33, s[0:1], 0x0
	s_min_i32 s0, s52, 0xc340
	s_ashr_i32 s1, s0, 31
	s_lshl_b64 s[0:1], s[0:1], 2
	s_add_u32 s0, s42, s0
	s_addc_u32 s1, s43, s1
	s_load_dword s53, s[0:1], 0x3c
	v_and_b32_e32 v1, 15, v0
	v_lshrrev_b32_e32 v19, 4, v0
	v_lshlrev_b32_e32 v20, 4, v1
	s_waitcnt lgkmcnt(0)
	s_cmp_ge_i32 s33, s53
	s_nop 0
	s_cbranch_scc1 .Lagg3_empty
	v_mov_b32_e32 v2, 0x4400
	v_lshl_or_b32 v40, v0, 2, v2
	v_lshl_or_b32 v41, v19, 2, v2
	v_mov_b32_e32 v2, 0x2200
	v_or_b32_e32 v21, 0x3400, v20
	v_cmp_eq_u32_e64 s[0:1], 0, v1
	v_cmp_eq_u32_e64 s[2:3], 1, v19
	v_cmp_eq_u32_e64 s[4:5], 2, v19
	v_cmp_eq_u32_e64 s[6:7], 3, v19
	v_cmp_eq_u32_e64 s[8:9], 4, v19
	v_cmp_eq_u32_e64 s[10:11], 5, v19
	v_cmp_eq_u32_e64 s[12:13], 6, v19
	v_cmp_eq_u32_e64 s[14:15], 7, v19
	v_cmp_eq_u32_e64 s[16:17], 8, v19
	v_cmp_eq_u32_e64 s[18:19], 9, v19
	v_cmp_eq_u32_e64 s[20:21], 10, v19
	v_cmp_eq_u32_e64 s[22:23], 11, v19
	v_cmp_eq_u32_e64 s[24:25], 12, v19
	v_cmp_eq_u32_e64 s[26:27], 13, v19
	v_cmp_eq_u32_e64 s[28:29], 14, v19
	v_cmp_eq_u32_e64 s[30:31], 15, v19
	v_add_u32_e32 v22, s33, v0
	v_lshl_add_u32 v42, v0, 3, v2
	v_mov_b32_e32 v43, 0
	s_movk_i32 s66, 0x110
	v_mov_b32_e32 v44, -1
	s_mov_b64 s[40:41], 0x800
	s_mov_b32 s67, 0xffff0
	s_mov_b32 s68, s33
	s_branch .LBB3_8

.Lagg4_nospecb:
	s_mov_b64 exec, s[4:5]
	global_load_dwordx2 v[8:9], v[8:9], off
	s_add_u32 s0, s40, s0
	s_addc_u32 s1, s41, s1
	s_load_dword s33, s[0:1], 0x0
	s_min_i32 s0, s50, 0xc340
	s_ashr_i32 s1, s0, 31
	s_lshl_b64 s[0:1], s[0:1], 2
	s_add_u32 s0, s42, s0
	s_addc_u32 s1, s43, s1
	s_load_dword s51, s[0:1], 0x3c
	v_and_b32_e32 v1, 15, v0
	v_lshrrev_b32_e32 v38, 4, v0
	v_lshlrev_b32_e32 v18, 4, v1
	s_waitcnt lgkmcnt(0)
	s_cmp_ge_i32 s33, s51
	s_nop 0
	s_cbranch_scc1 .Lagg4_empty
	v_mov_b32_e32 v2, 0x4400
	v_lshl_or_b32 v40, v0, 2, v2
	v_lshl_or_b32 v41, v38, 2, v2
	v_mov_b32_e32 v2, 0x2200
	v_or_b32_e32 v39, 0x3400, v18
	v_cmp_eq_u32_e64 s[0:1], 0, v1
	v_cmp_eq_u32_e64 s[2:3], 1, v38
	v_cmp_eq_u32_e64 s[4:5], 2, v38
	v_cmp_eq_u32_e64 s[6:7], 3, v38
	v_cmp_eq_u32_e64 s[8:9], 4, v38
	v_cmp_eq_u32_e64 s[10:11], 5, v38
	v_cmp_eq_u32_e64 s[12:13], 6, v38
	v_cmp_eq_u32_e64 s[14:15], 7, v38
	v_cmp_eq_u32_e64 s[16:17], 8, v38
	v_cmp_eq_u32_e64 s[18:19], 9, v38
	v_cmp_eq_u32_e64 s[20:21], 10, v38
	v_cmp_eq_u32_e64 s[22:23], 11, v38
	v_cmp_eq_u32_e64 s[24:25], 12, v38
	v_cmp_eq_u32_e64 s[26:27], 13, v38
	v_cmp_eq_u32_e64 s[28:29], 14, v38
	v_cmp_eq_u32_e64 s[30:31], 15, v38
	v_add_u32_e32 v20, s33, v0
	v_lshl_add_u32 v42, v0, 3, v2
	v_mov_b32_e32 v43, 0
	s_movk_i32 s64, 0x110
	v_mov_b32_e32 v44, -1
	s_mov_b64 s[40:41], 0x800
	s_mov_b32 s65, 0xffff0
	s_mov_b32 s66, s33
	s_branch .LBB4_8
